# LDS-DMA global addresses formed on the scalar unit (saddr form, lane*16 in one VGPR) in the MLA, DIFF and GQA loops: 2-3 64-bit VALU adds per tile removed
# speedup vs baseline: 1.0016x; 1.0014x over previous
.LBB0_922:
	s_mul_hi_i32 s31, s29, 0x208000
	s_mul_i32 s29, s29, 0x208000
	s_add_u32 s30, s18, s29
	s_addc_u32 s31, s19, s31
	s_add_u32 s34, s30, s25
	s_addc_u32 s35, s31, s26
	s_add_i32 m0, s27, 0x3000
	s_add_u32 s33, s22, 0x3000
	s_mov_b32 s56, s34
	s_mov_b32 s57, s35
	v_lshl_add_u64 v[214:215], s[34:35], 0, v[0:1]
	s_addc_u32 s34, s23, 0
	s_add_u32 s38, s33, s25
	s_addc_u32 s39, s34, s26
	global_load_lds_dwordx4 v[214:215], off
	v_lshl_add_u64 v[6:7], s[38:39], 0, v[0:1]
	s_add_i32 m0, s27, 0x5000
	s_andn2_b64 vcc, exec, s[12:13]
	global_load_lds_dwordx4 v[6:7], off
	s_mov_b64 s[12:13], -1
	s_cbranch_vccnz .LBB0_924
	s_ashr_i32 s29, s28, 31
	s_mov_b64 s[12:13], 0

.LBB0_927:
	s_min_i32 s34, s31, 0x101
	s_add_i32 s88, s34, 2
	s_mul_i32 s34, s88, 0x3000
	s_add_u32 s35, s22, s34
	s_addc_u32 s38, s23, 0
	s_add_u32 s40, s35, s25
	s_mul_i32 s34, s13, 0x5000
	s_addc_u32 s41, s38, s26
	s_add_i32 s34, s27, s34
	s_mov_b32 m0, s34
	s_andn2_b64 vcc, exec, s[10:11]
	global_load_lds_dwordx4 v0, s[40:41]
	s_cbranch_vccnz .LBB0_929
	s_add_u32 s40, s35, s28
	s_addc_u32 s41, s38, s29
	s_add_i32 m0, s34, 0x2000
	s_nop 0
	global_load_lds_dwordx4 v0, s[40:41]
.LBB0_929:
	s_lshl_b64 s[38:39], s[88:89], 13
	s_add_u32 s60, s56, s38
	s_addc_u32 s61, s57, s39
	s_add_i32 m0, s34, 0x3000
	s_mul_i32 s34, s30, 0x5000
	global_load_lds_dwordx4 v0, s[60:61]
	s_add_i32 s34, s34, 0
	v_add_u32_e32 v224, s34, v231
	s_mul_i32 s35, s12, 0x5000
	s_mulk_i32 s33, 0x5000
	v_add_u32_e32 v235, s34, v233
	v_add_u32_e32 v210, s35, v232
	v_add_u32_e32 v225, s33, v234
	ds_read_b128 v[216:219], v224 offset:4608
	v_mfma_f32_32x32x16_bf16 v[114:129], v[240:243], v[130:133], 0
	v_exp_f32_e32 v82, v82
	v_exp_f32_e32 v83, v83
	v_exp_f32_e32 v84, v84
	v_mfma_f32_32x32x16_bf16 v[98:113], v[240:243], v[170:173], 0
	ds_read_b128 v[220:223], v224 offset:6656
	v_exp_f32_e32 v85, v85
	v_cvt_pk_bf16_f32 v198, v82, v83
	v_add_f32_e32 v212, v82, v212
	v_add_f32_e32 v212, v83, v212
	v_mfma_f32_32x32x16_bf16 v[114:129], v[244:247], v[134:137], v[114:129]
	v_exp_f32_e32 v86, v86
	v_exp_f32_e32 v87, v87
	v_cvt_pk_bf16_f32 v199, v84, v85
	v_add_f32_e32 v212, v84, v212
	v_mfma_f32_32x32x16_bf16 v[98:113], v[244:247], v[138:141], v[98:113]
	ds_read_b128 v[240:243], v224 offset:8704
	v_add_f32_e32 v212, v85, v212
	v_exp_f32_e32 v88, v88
	v_exp_f32_e32 v89, v89
	s_waitcnt lgkmcnt(2)
	v_mfma_f32_32x32x16_bf16 v[114:129], v[216:219], v[146:149], v[114:129]
	v_cvt_pk_bf16_f32 v200, v86, v87
	v_add_f32_e32 v212, v86, v212
	v_add_f32_e32 v212, v87, v212
	v_exp_f32_e32 v90, v90
	v_exp_f32_e32 v91, v91
	v_mfma_f32_32x32x16_bf16 v[98:113], v[216:219], v[142:145], v[98:113]
	ds_read_b128 v[244:247], v224 offset:10752
	v_cvt_pk_bf16_f32 v201, v88, v89
	v_add_f32_e32 v212, v88, v212
	v_add_f32_e32 v212, v89, v212
	v_exp_f32_e32 v92, v92
	s_waitcnt lgkmcnt(2)
	v_mfma_f32_32x32x16_bf16 v[114:129], v[220:223], v[150:153], v[114:129]
	v_exp_f32_e32 v93, v93
	v_cvt_pk_bf16_f32 v194, v90, v91
	v_add_f32_e32 v212, v90, v212
	v_add_f32_e32 v212, v91, v212
	v_mfma_f32_32x32x16_bf16 v[98:113], v[220:223], v[154:157], v[98:113]
	ds_read_b128 v[216:219], v225 offset:16384
	v_exp_f32_e32 v94, v94
	v_exp_f32_e32 v95, v95
	v_cvt_pk_bf16_f32 v195, v92, v93
	v_add_f32_e32 v212, v92, v212
	s_waitcnt lgkmcnt(2)
	v_mfma_f32_32x32x16_bf16 v[114:129], v[240:243], v[162:165], v[114:129]
	v_add_f32_e32 v212, v93, v212
	v_exp_f32_e32 v96, v96
	v_exp_f32_e32 v97, v97
	v_mfma_f32_32x32x16_bf16 v[98:113], v[240:243], v[158:161], v[98:113]
	ds_read_b128 v[220:223], v225 offset:16896
	v_cvt_pk_bf16_f32 v196, v94, v95
	v_add_f32_e32 v212, v94, v212
	v_add_f32_e32 v212, v95, v212
	v_exp_f32_e32 v66, v66
	v_exp_f32_e32 v67, v67
	s_waitcnt lgkmcnt(2)
	v_mfma_f32_32x32x16_bf16 v[114:129], v[244:247], v[166:169], v[114:129]
	v_cvt_pk_bf16_f32 v197, v96, v97
	v_add_f32_e32 v212, v96, v212
	v_add_f32_e32 v212, v97, v212
	v_exp_f32_e32 v68, v68
	v_mfma_f32_32x32x16_bf16 v[98:113], v[244:247], v[174:177], v[98:113]
	v_exp_f32_e32 v69, v69
	v_cvt_pk_bf16_f32 v202, v66, v67
	v_add_f32_e32 v213, v66, v213
	v_add_f32_e32 v213, v67, v213
	s_waitcnt lgkmcnt(1)
	v_mfma_f32_32x32x16_bf16 v[18:33], v[216:219], v[178:181], v[18:33]
	ds_read_b128 v[240:243], v225 offset:18432
	v_exp_f32_e32 v70, v70
	v_exp_f32_e32 v71, v71
	v_cvt_pk_bf16_f32 v203, v68, v69
	v_add_f32_e32 v213, v68, v213
	s_waitcnt lgkmcnt(1)
	v_mfma_f32_32x32x16_bf16 v[34:49], v[220:223], v[178:181], v[34:49]
	ds_read_b128 v[244:247], v225 offset:18944
	v_add_f32_e32 v213, v69, v213
	v_exp_f32_e32 v72, v72
	v_exp_f32_e32 v73, v73
	v_mfma_f32_32x32x16_bf16 v[50:65], v[216:219], v[190:193], v[50:65]
	v_cvt_pk_bf16_f32 v204, v70, v71
	v_add_f32_e32 v213, v70, v213
	v_add_f32_e32 v213, v71, v213
	v_exp_f32_e32 v74, v74
	v_exp_f32_e32 v75, v75
	v_mfma_f32_32x32x16_bf16 v[2:17], v[220:223], v[190:193], v[2:17]
	v_cvt_pk_bf16_f32 v205, v72, v73
	v_add_f32_e32 v213, v72, v213
	v_add_f32_e32 v213, v73, v213
	v_exp_f32_e32 v76, v76
	s_waitcnt lgkmcnt(1)
	v_mfma_f32_32x32x16_bf16 v[18:33], v[240:243], v[182:185], v[18:33]
	ds_read_b128 v[216:219], v210
	v_exp_f32_e32 v77, v77
	v_cvt_pk_bf16_f32 v206, v74, v75
	v_add_f32_e32 v213, v74, v213
	v_add_f32_e32 v213, v75, v213
	s_waitcnt lgkmcnt(1)
	v_mfma_f32_32x32x16_bf16 v[34:49], v[244:247], v[182:185], v[34:49]
	v_exp_f32_e32 v78, v78
	v_exp_f32_e32 v79, v79
	v_cvt_pk_bf16_f32 v207, v76, v77
	v_add_f32_e32 v213, v76, v213
	v_mfma_f32_32x32x16_bf16 v[50:65], v[240:243], v[186:189], v[50:65]
	ds_read_b128 v[220:223], v210 offset:2048
	v_add_f32_e32 v213, v77, v213
	v_exp_f32_e32 v80, v80
	v_exp_f32_e32 v81, v81
	v_mfma_f32_32x32x16_bf16 v[2:17], v[244:247], v[186:189], v[2:17]
	v_cvt_pk_bf16_f32 v208, v78, v79
	v_add_f32_e32 v213, v78, v213
	v_add_f32_e32 v213, v79, v213
	v_cvt_pk_bf16_f32 v209, v80, v81
	v_add_f32_e32 v213, v80, v213
	v_add_f32_e32 v213, v81, v213
	s_waitcnt lgkmcnt(1)
	v_mfma_f32_32x32x16_bf16 v[82:97], v[216:219], v[130:133], 0
	ds_read_b128 v[240:243], v210 offset:4096
	v_exp_f32_e32 v114, v114
	v_exp_f32_e32 v115, v115
	v_exp_f32_e32 v116, v116
	v_mfma_f32_32x32x16_bf16 v[66:81], v[216:219], v[170:173], 0
	v_exp_f32_e32 v117, v117
	v_cvt_pk_bf16_f32 v178, v114, v115
	v_add_f32_e32 v212, v114, v212
	v_add_f32_e32 v212, v115, v212
	s_waitcnt lgkmcnt(1)
	v_mfma_f32_32x32x16_bf16 v[82:97], v[220:223], v[134:137], v[82:97]
	ds_read_b128 v[244:247], v210 offset:6144
	v_exp_f32_e32 v118, v118
	v_exp_f32_e32 v119, v119
	v_cvt_pk_bf16_f32 v179, v116, v117
	v_add_f32_e32 v212, v116, v212
	v_mfma_f32_32x32x16_bf16 v[66:81], v[220:223], v[138:141], v[66:81]
	v_add_f32_e32 v212, v117, v212
	v_exp_f32_e32 v120, v120
	v_exp_f32_e32 v121, v121
	s_waitcnt lgkmcnt(1)
	v_mfma_f32_32x32x16_bf16 v[82:97], v[240:243], v[146:149], v[82:97]
	ds_read_b128 v[216:219], v210 offset:8192
	v_cvt_pk_bf16_f32 v180, v118, v119
	v_add_f32_e32 v212, v118, v212
	v_add_f32_e32 v212, v119, v212
	v_exp_f32_e32 v122, v122
	v_exp_f32_e32 v123, v123
	v_mfma_f32_32x32x16_bf16 v[66:81], v[240:243], v[142:145], v[66:81]
	v_cvt_pk_bf16_f32 v181, v120, v121
	v_add_f32_e32 v212, v120, v212
	v_add_f32_e32 v212, v121, v212
	v_exp_f32_e32 v124, v124
	s_waitcnt lgkmcnt(1)
	v_mfma_f32_32x32x16_bf16 v[82:97], v[244:247], v[150:153], v[82:97]
	ds_read_b128 v[220:223], v210 offset:10240
	v_exp_f32_e32 v125, v125
	v_cvt_pk_bf16_f32 v182, v122, v123
	v_add_f32_e32 v212, v122, v212
	v_add_f32_e32 v212, v123, v212
	v_mfma_f32_32x32x16_bf16 v[66:81], v[244:247], v[154:157], v[66:81]
	v_exp_f32_e32 v126, v126
	v_exp_f32_e32 v127, v127
	v_cvt_pk_bf16_f32 v183, v124, v125
	v_add_f32_e32 v212, v124, v212
	s_waitcnt lgkmcnt(1)
	v_mfma_f32_32x32x16_bf16 v[82:97], v[216:219], v[162:165], v[82:97]
	ds_read_b128 v[240:243], v235 offset:12288
	v_add_f32_e32 v212, v125, v212
	v_exp_f32_e32 v128, v128
	v_exp_f32_e32 v129, v129
	v_mfma_f32_32x32x16_bf16 v[66:81], v[216:219], v[158:161], v[66:81]
	ds_read_b128 v[244:247], v235 offset:12800
	v_cvt_pk_bf16_f32 v184, v126, v127
	v_add_f32_e32 v212, v126, v212
	v_add_f32_e32 v212, v127, v212
	v_exp_f32_e32 v98, v98
	v_exp_f32_e32 v99, v99
	s_waitcnt lgkmcnt(2)
	v_mfma_f32_32x32x16_bf16 v[82:97], v[220:223], v[166:169], v[82:97]
	v_cvt_pk_bf16_f32 v185, v128, v129
	v_add_f32_e32 v212, v128, v212
	v_add_f32_e32 v212, v129, v212
	v_exp_f32_e32 v100, v100
	v_mfma_f32_32x32x16_bf16 v[66:81], v[220:223], v[174:177], v[66:81]
	v_exp_f32_e32 v101, v101
	v_cvt_pk_bf16_f32 v190, v98, v99
	v_add_f32_e32 v213, v98, v213
	v_add_f32_e32 v213, v99, v213
	s_waitcnt lgkmcnt(1)
	v_mfma_f32_32x32x16_bf16 v[18:33], v[240:243], v[198:201], v[18:33]
	ds_read_b128 v[216:219], v235 offset:14336
	v_exp_f32_e32 v102, v102
	v_exp_f32_e32 v103, v103
	v_cvt_pk_bf16_f32 v191, v100, v101
	v_add_f32_e32 v213, v100, v213
	s_waitcnt lgkmcnt(1)
	v_mfma_f32_32x32x16_bf16 v[34:49], v[244:247], v[198:201], v[34:49]
	ds_read_b128 v[220:223], v235 offset:14848
	v_add_f32_e32 v213, v101, v213
	v_exp_f32_e32 v104, v104
	v_exp_f32_e32 v105, v105
	v_mfma_f32_32x32x16_bf16 v[50:65], v[240:243], v[202:205], v[50:65]
	v_cvt_pk_bf16_f32 v192, v102, v103
	v_add_f32_e32 v213, v102, v213
	v_add_f32_e32 v213, v103, v213
	v_exp_f32_e32 v106, v106
	v_exp_f32_e32 v107, v107
	v_mfma_f32_32x32x16_bf16 v[2:17], v[244:247], v[202:205], v[2:17]
	v_cvt_pk_bf16_f32 v193, v104, v105
	v_add_f32_e32 v213, v104, v213
	v_add_f32_e32 v213, v105, v213
	v_exp_f32_e32 v108, v108
	s_waitcnt lgkmcnt(1)
	v_mfma_f32_32x32x16_bf16 v[18:33], v[216:219], v[194:197], v[18:33]
	ds_read_b128 v[240:243], v210 offset:512
	v_exp_f32_e32 v109, v109
	v_cvt_pk_bf16_f32 v186, v106, v107
	v_add_f32_e32 v213, v106, v213
	v_add_f32_e32 v213, v107, v213
	s_waitcnt lgkmcnt(1)
	v_mfma_f32_32x32x16_bf16 v[34:49], v[220:223], v[194:197], v[34:49]
	v_exp_f32_e32 v110, v110
	v_exp_f32_e32 v111, v111
	v_cvt_pk_bf16_f32 v187, v108, v109
	v_add_f32_e32 v213, v108, v213
	v_mfma_f32_32x32x16_bf16 v[50:65], v[216:219], v[206:209], v[50:65]
	ds_read_b128 v[244:247], v210 offset:2560
	v_add_f32_e32 v213, v109, v213
	v_exp_f32_e32 v112, v112
	v_exp_f32_e32 v113, v113
	v_mfma_f32_32x32x16_bf16 v[2:17], v[220:223], v[206:209], v[2:17]
	v_cvt_pk_bf16_f32 v188, v110, v111
	v_add_f32_e32 v213, v110, v213
	v_add_f32_e32 v213, v111, v213
	v_cvt_pk_bf16_f32 v189, v112, v113
	v_add_f32_e32 v213, v112, v213
	v_add_f32_e32 v213, v113, v213
	s_add_i32 s33, s13, 1
	s_waitcnt vmcnt(0)
	s_and_b32 s34, s33, 3
	s_add_i32 s31, s31, 1
	s_cmpk_eq_i32 s31, 0x104
	s_waitcnt vmcnt(0) lgkmcnt(0)
	s_barrier
	s_cbranch_scc1 .LBB0_931
	s_mov_b32 s33, s30
	s_mov_b32 s30, s12
	s_mov_b32 s12, s13
	s_mov_b32 s13, s34
	s_branch .LBB0_927

.LBB0_952:
	s_lshr_b32 s11, s19, 3
	s_and_b32 s10, s19, 31
	s_and_b32 s11, s11, 0xffffe0
	s_or_b32 s10, s11, s10
	s_bfe_u32 s25, s19, 0x10007
	s_lshl_b32 s10, s10, 8
	s_bfe_u32 s26, s19, 0x20005
	s_lshl_b32 s11, s25, 14
	s_ashr_i32 s20, s10, 31
	s_add_u32 s10, s10, s11
	s_addc_u32 s11, s20, 0
	s_lshl_b64 s[20:21], s[10:11], 9
	s_add_u32 s22, s12, s20
	s_addc_u32 s21, s13, s21
	s_lshl_b32 s20, s26, 6
	s_lshl_b32 s23, s26, 7
	s_add_u32 s22, s22, s23
	s_addc_u32 s23, s21, 0
	s_lshl_b32 s21, s25, 2
	s_or_b32 s21, s21, s26
	s_mul_i32 s21, s21, 0x208000
	s_add_u32 s25, s14, s21
	s_addc_u32 s26, s15, 0
	v_mov_b32_e32 v4, v230
	s_add_u32 s27, s16, s21
	s_addc_u32 s28, s17, 0
	v_readfirstlane_b32 s21, v4
	v_and_b32_e32 v18, 31, v4
	s_ashr_i32 s21, s21, 6
	s_cmp_lt_i32 s21, 8
	v_lshl_or_b32 v0, s21, 5, v18
	v_ashrrev_i32_e32 v2, 31, v0
	s_cselect_b64 vcc, -1, 0
	v_cndmask_b32_e32 v3, 0, v2, vcc
	v_cndmask_b32_e32 v2, v18, v0, vcc
	v_bfe_u32 v5, v4, 5, 1
	v_lshlrev_b64 v[2:3], 9, v[2:3]
	v_lshl_add_u64 v[2:3], s[22:23], 0, v[2:3]
	v_lshlrev_b32_e32 v0, 4, v5
	v_lshl_add_u64 v[2:3], v[2:3], 0, v[0:1]
	global_load_dwordx4 v[130:133], v[2:3], off
	global_load_dwordx4 v[134:137], v[2:3], off offset:64
	global_load_dwordx4 v[138:141], v[2:3], off offset:32
	global_load_dwordx4 v[142:145], v[2:3], off offset:96
	s_lshl_b32 s29, s21, 10
	s_ashr_i32 s30, s29, 31
	v_and_b32_e32 v0, 63, v4
	v_and_b32_e32 v2, 19, v4
	v_lshlrev_b32_e32 v3, 1, v4
	v_lshrrev_b32_e32 v4, 1, v4
	s_add_u32 s22, s25, s29
	v_and_b32_e32 v3, 8, v3
	v_and_b32_e32 v4, 4, v4
	s_addc_u32 s23, s26, s30
	s_add_i32 s21, s29, 0
	v_lshlrev_b32_e32 v19, 10, v5
	v_or3_b32 v2, v2, v3, v4
	v_lshlrev_b32_e32 v0, 4, v0
	s_add_u32 s26, s27, s29
	s_mov_b32 m0, s21
	v_lshl_or_b32 v2, v2, 4, v19
	s_mov_b32 s56, s22
	s_mov_b32 s57, s23
	v_lshl_add_u64 v[174:175], s[22:23], 0, v[0:1]
	global_load_lds_dwordx4 v0, s[22:23]
	s_addc_u32 s27, s28, s30
	s_add_i32 m0, s21, 0x2000
	s_mov_b64 s[22:23], 0x2000
	v_add_u32_e32 v188, 0, v2
	s_mov_b32 s58, s26
	s_mov_b32 s59, s27
	v_lshl_add_u64 v[176:177], s[26:27], 0, v[0:1]
	global_load_lds_dwordx4 v0, s[26:27]
	v_lshl_add_u64 v[2:3], v[174:175], 0, s[22:23]
	s_add_i32 m0, s21, 0x4000
	v_mov_b32_e32 v150, v1
	global_load_lds_dwordx4 v[2:3], off
	v_lshl_add_u64 v[2:3], v[176:177], 0, s[22:23]
	s_add_i32 m0, s21, 0x6000
	v_lshl_or_b32 v0, v18, 4, v19
	global_load_lds_dwordx4 v[2:3], off
	s_waitcnt vmcnt(0)
	s_waitcnt vmcnt(0) lgkmcnt(0)
	s_barrier
	ds_read_b128 v[2:5], v188
	ds_read_b128 v[6:9], v188 offset:4096
	ds_read_b128 v[98:101], v188 offset:512
	ds_read_b128 v[10:13], v188 offset:2048
	ds_read_b128 v[102:105], v188 offset:4608
	ds_read_b128 v[14:17], v188 offset:6144
	ds_read_b128 v[162:165], v188 offset:2560
	ds_read_b128 v[166:169], v188 offset:6656
	s_mov_b32 s22, 2
	s_mov_b32 s23, 1
	s_mov_b32 s27, 0
	s_mov_b32 s25, 0
	s_mov_b32 s26, 0
	v_add_u32_e32 v0, 0, v0
	v_mov_b32_e32 v151, v150
	v_mov_b32_e32 v152, v150
	v_mov_b32_e32 v153, v150
	v_mov_b32_e32 v154, v150
	v_mov_b32_e32 v155, v150
	v_mov_b32_e32 v156, v150
	v_mov_b32_e32 v157, v150
	s_waitcnt lgkmcnt(7)
	v_mfma_f32_32x32x16_bf16 v[82:97], v[2:5], v[130:133], 0
	v_mov_b32_e32 v2, 0
	v_mov_b32_e32 v3, v2
	v_mov_b32_e32 v4, v2
	v_mov_b32_e32 v5, v2
	v_mov_b32_e32 v18, v2
	v_mov_b32_e32 v19, v2
	v_mov_b32_e32 v20, v2
	s_waitcnt lgkmcnt(6)
	v_mfma_f32_32x32x16_bf16 v[66:81], v[6:9], v[134:137], 0
	v_mov_b32_e32 v6, v2
	v_mov_b32_e32 v7, v2
	v_mov_b32_e32 v8, v2
	v_mov_b32_e32 v9, v2
	v_mov_b32_e32 v21, v2
	v_mov_b32_e32 v22, v2
	v_mov_b32_e32 v23, v2
	s_waitcnt lgkmcnt(4)
	v_mfma_f32_32x32x16_bf16 v[82:97], v[10:13], v[138:141], v[82:97]
	v_mov_b32_e32 v10, v2
	v_mov_b32_e32 v11, v2
	v_mov_b32_e32 v12, v2
	v_mov_b32_e32 v13, v2
	v_mov_b32_e32 v24, v2
	v_mov_b32_e32 v25, v2
	v_mov_b32_e32 v26, v2
	s_waitcnt lgkmcnt(2)
	v_mfma_f32_32x32x16_bf16 v[66:81], v[14:17], v[142:145], v[66:81]
	v_mov_b32_e32 v14, v2
	v_mov_b32_e32 v15, v2
	v_mov_b32_e32 v16, v2
	v_mov_b32_e32 v17, v2
	v_mov_b32_e32 v27, v2
	v_mov_b32_e32 v28, v2
	v_mov_b32_e32 v29, v2
	v_mov_b32_e32 v30, v2
	v_mov_b32_e32 v31, v2
	v_mov_b32_e32 v32, v2
	v_mov_b32_e32 v33, v2
	v_mov_b32_e32 v158, v150
	v_mov_b32_e32 v159, v150
	v_mov_b32_e32 v160, v150
	v_mov_b32_e32 v161, v150
	v_mov_b32_e32 v146, v150
	v_mov_b32_e32 v147, v150
	v_mov_b32_e32 v148, v150
	v_mov_b32_e32 v149, v150
	v_mov_b32_e32 v34, v2
	v_mov_b32_e32 v35, v2
	v_mov_b32_e32 v36, v2
	v_mov_b32_e32 v37, v2
	v_mov_b32_e32 v38, v2
	v_mov_b32_e32 v39, v2
	v_mov_b32_e32 v40, v2
	v_mov_b32_e32 v41, v2
	v_mov_b32_e32 v42, v2
	v_mov_b32_e32 v43, v2
	v_mov_b32_e32 v44, v2
	v_mov_b32_e32 v45, v2
	v_mov_b32_e32 v46, v2
	v_mov_b32_e32 v47, v2
	v_mov_b32_e32 v48, v2
	v_mov_b32_e32 v49, v2
	v_mov_b32_e32 v50, v2
	v_mov_b32_e32 v51, v2
	v_mov_b32_e32 v52, v2
	v_mov_b32_e32 v53, v2
	v_mov_b32_e32 v54, v2
	v_mov_b32_e32 v55, v2
	v_mov_b32_e32 v56, v2
	v_mov_b32_e32 v57, v2
	v_mov_b32_e32 v58, v2
	v_mov_b32_e32 v59, v2
	v_mov_b32_e32 v60, v2
	v_mov_b32_e32 v61, v2
	v_mov_b32_e32 v62, v2
	v_mov_b32_e32 v63, v2
	v_mov_b32_e32 v64, v2
	v_mov_b32_e32 v65, v2
	v_mov_b32_e32 v178, v2
	v_mov_b32_e32 v179, v2
	v_mov_b32_e32 v234, 0
	v_mov_b32_e32 v235, 0
	v_mbcnt_lo_u32_b32 v174, -1, 0
	v_mbcnt_hi_u32_b32 v174, -1, v174
	v_lshlrev_b32_e32 v174, 4, v174
.LBB0_953:
	v_mfma_f32_32x32x16_bf16 v[114:129], v[98:101], v[130:133], 0
	s_min_i32 s28, s26, 0x101
	s_lshl_b32 s28, s28, 13
	s_add_i32 s88, s28, 0x4000
	s_lshl_b32 s28, s22, 14
	s_add_i32 s28, s21, s28
	s_add_u32 s60, s56, s88
	s_addc_u32 s61, s57, s89
	s_mov_b32 m0, s28
	v_lshl_add_u32 v181, s27, 14, v0
	global_load_lds_dwordx4 v174, s[60:61]
	s_add_u32 s62, s58, s88
	s_addc_u32 s63, s59, s89
	s_add_i32 m0, s28, 0x2000
	s_lshl_b32 s28, s25, 14
	global_load_lds_dwordx4 v174, s[62:63]
	ds_read_b128 v[190:193], v181 offset:12288
	v_add_u32_e32 v189, s28, v0
	v_lshl_add_u32 v210, s23, 14, v188
	v_exp_f32_e32 v194, v82
	v_exp_f32_e32 v196, v83
	v_exp_f32_e32 v198, v84
	v_exp_f32_e32 v200, v85
	v_mfma_f32_32x32x16_bf16 v[98:113], v[102:105], v[134:137], 0
	ds_read_b128 v[82:85], v181 offset:12800
	v_cvt_pk_bf16_f32 v170, v194, v196
	v_cvt_pk_bf16_f32 v171, v198, v200
	v_exp_f32_e32 v202, v86
	v_exp_f32_e32 v204, v87
	s_waitcnt lgkmcnt(0)
	v_mfma_f32_32x32x16_bf16 v[114:129], v[162:165], v[138:141], v[114:129]
	v_cvt_pk_bf16_f32 v172, v202, v204
	v_exp_f32_e32 v206, v88
	v_exp_f32_e32 v208, v89
	v_mfma_f32_32x32x16_bf16 v[98:113], v[166:169], v[142:145], v[98:113]
	v_exp_f32_e32 v168, v92
	v_exp_f32_e32 v166, v93
	v_cvt_pk_bf16_f32 v173, v206, v208
	v_exp_f32_e32 v214, v90
	v_exp_f32_e32 v216, v91
	v_mfma_f32_32x32x16_bf16 v[34:49], v[190:193], v[150:153], v[34:49]
	ds_read_b128 v[86:89], v181 offset:14336
	v_cvt_pk_bf16_f32 v162, v214, v216
	v_cvt_pk_bf16_f32 v163, v168, v166
	v_exp_f32_e32 v182, v94
	v_exp_f32_e32 v180, v95
	v_mfma_f32_32x32x16_bf16 v[50:65], v[82:85], v[150:153], v[50:65]
	ds_read_b128 v[90:93], v181 offset:14848
	v_cvt_pk_bf16_f32 v164, v182, v180
	v_exp_f32_e32 v186, v96
	v_exp_f32_e32 v184, v97
	v_mfma_f32_32x32x16_bf16 v[2:17], v[190:193], v[158:161], v[2:17]
	v_cvt_pk_bf16_f32 v165, v186, v184
	v_exp_f32_e32 v195, v66
	v_exp_f32_e32 v197, v67
	v_exp_f32_e32 v199, v68
	v_exp_f32_e32 v201, v69
	v_mfma_f32_32x32x16_bf16 v[18:33], v[82:85], v[158:161], v[18:33]
	v_cvt_pk_bf16_f32 v158, v195, v197
	v_cvt_pk_bf16_f32 v159, v199, v201
	v_exp_f32_e32 v203, v70
	v_exp_f32_e32 v205, v71
	s_waitcnt lgkmcnt(0)
	v_mfma_f32_32x32x16_bf16 v[34:49], v[86:89], v[154:157], v[34:49]
	ds_read_b128 v[66:69], v210
	v_cvt_pk_bf16_f32 v160, v203, v205
	v_exp_f32_e32 v207, v72
	v_exp_f32_e32 v209, v73
	v_mfma_f32_32x32x16_bf16 v[50:65], v[90:93], v[154:157], v[50:65]
	ds_read_b128 v[70:73], v210 offset:4096
	v_exp_f32_e32 v169, v76
	v_exp_f32_e32 v167, v77
	v_cvt_pk_bf16_f32 v161, v207, v209
	v_exp_f32_e32 v215, v74
	v_exp_f32_e32 v217, v75
	v_pk_add_f32 v[74:75], v[178:179], v[194:195]
	v_mfma_f32_32x32x16_bf16 v[2:17], v[86:89], v[146:149], v[2:17]
	v_add_f32_e64 v74, v196, v74
	v_add_f32_e64 v75, v197, v75
	ds_read_b128 v[152:155], v210 offset:2048
	v_add_f32_e64 v74, v198, v74
	v_add_f32_e64 v75, v199, v75
	v_cvt_pk_bf16_f32 v190, v215, v217
	v_pk_add_f32 v[234:235], v[200:201], v[234:235]
	v_cvt_pk_bf16_f32 v191, v169, v167
	v_pk_add_f32 v[74:75], v[202:203], v[74:75]
	v_exp_f32_e32 v183, v78
	v_pk_add_f32 v[234:235], v[204:205], v[234:235]
	v_exp_f32_e32 v181, v79
	v_pk_add_f32 v[74:75], v[206:207], v[74:75]
	v_pk_add_f32 v[234:235], v[208:209], v[234:235]
	v_pk_add_f32 v[74:75], v[214:215], v[74:75]
	s_nop 0
	v_pk_add_f32 v[178:179], v[216:217], v[74:75]
	v_mfma_f32_32x32x16_bf16 v[18:33], v[90:93], v[146:149], v[18:33]
	v_exp_f32_e32 v187, v80
	v_exp_f32_e32 v185, v81
	ds_read_b128 v[194:197], v210 offset:6144
	v_cvt_pk_bf16_f32 v192, v183, v181
	v_cvt_pk_bf16_f32 v193, v187, v185
	s_waitcnt lgkmcnt(0)
	v_mfma_f32_32x32x16_bf16 v[82:97], v[66:69], v[130:133], 0
	ds_read_b128 v[146:149], v189 offset:8192
	v_exp_f32_e32 v198, v114
	v_exp_f32_e32 v200, v115
	v_exp_f32_e32 v202, v116
	v_exp_f32_e32 v204, v117
	v_mfma_f32_32x32x16_bf16 v[66:81], v[70:73], v[134:137], 0
	ds_read_b128 v[114:117], v189 offset:8704
	v_cvt_pk_bf16_f32 v150, v198, v200
	v_cvt_pk_bf16_f32 v151, v202, v204
	v_exp_f32_e32 v206, v118
	v_exp_f32_e32 v208, v119
	v_mfma_f32_32x32x16_bf16 v[82:97], v[152:155], v[138:141], v[82:97]
	v_cvt_pk_bf16_f32 v152, v206, v208
	v_exp_f32_e32 v214, v120
	v_exp_f32_e32 v216, v121
	v_mfma_f32_32x32x16_bf16 v[66:81], v[194:197], v[142:145], v[66:81]
	v_cvt_pk_bf16_f32 v153, v214, v216
	v_exp_f32_e32 v194, v122
	v_exp_f32_e32 v196, v123
	v_exp_f32_e32 v218, v124
	v_exp_f32_e32 v220, v125
	s_waitcnt lgkmcnt(0)
	v_mfma_f32_32x32x16_bf16 v[34:49], v[146:149], v[170:173], v[34:49]
	ds_read_b128 v[118:121], v189 offset:10240
	v_cvt_pk_bf16_f32 v154, v194, v196
	v_cvt_pk_bf16_f32 v155, v218, v220
	v_exp_f32_e32 v126, v126
	v_exp_f32_e32 v222, v127
	v_mfma_f32_32x32x16_bf16 v[50:65], v[114:117], v[170:173], v[50:65]
	ds_read_b128 v[122:125], v189 offset:10752
	v_cvt_pk_bf16_f32 v156, v126, v222
	v_exp_f32_e32 v128, v128
	v_exp_f32_e32 v170, v129
	v_mfma_f32_32x32x16_bf16 v[2:17], v[146:149], v[158:161], v[2:17]
	v_cvt_pk_bf16_f32 v157, v128, v170
	v_exp_f32_e32 v199, v98
	v_exp_f32_e32 v201, v99
	v_exp_f32_e32 v203, v100
	v_exp_f32_e32 v205, v101
	v_mfma_f32_32x32x16_bf16 v[18:33], v[114:117], v[158:161], v[18:33]
	v_cvt_pk_bf16_f32 v158, v199, v201
	v_cvt_pk_bf16_f32 v159, v203, v205
	v_exp_f32_e32 v207, v102
	v_exp_f32_e32 v209, v103
	v_pk_add_f32 v[102:103], v[168:169], v[178:179]
	s_waitcnt lgkmcnt(0)
	v_mfma_f32_32x32x16_bf16 v[34:49], v[118:121], v[162:165], v[34:49]
	v_add_f32_e64 v102, v166, v102
	v_add_f32_e64 v103, v167, v103
	ds_read_b128 v[98:101], v210 offset:512
	v_add_f32_e64 v102, v182, v102
	v_add_f32_e64 v103, v183, v103
	v_cvt_pk_bf16_f32 v160, v207, v209
	v_pk_add_f32 v[234:235], v[180:181], v[234:235]
	v_exp_f32_e32 v215, v104
	v_pk_add_f32 v[102:103], v[186:187], v[102:103]
	v_exp_f32_e32 v217, v105
	v_pk_add_f32 v[234:235], v[184:185], v[234:235]
	v_pk_add_f32 v[102:103], v[102:103], v[198:199]
	v_pk_add_f32 v[234:235], v[200:201], v[234:235]
	v_pk_add_f32 v[102:103], v[202:203], v[102:103]
	v_pk_add_f32 v[234:235], v[204:205], v[234:235]
	v_pk_add_f32 v[114:115], v[206:207], v[102:103]
	v_mfma_f32_32x32x16_bf16 v[50:65], v[122:125], v[162:165], v[50:65]
	ds_read_b128 v[102:105], v210 offset:4608
	v_cvt_pk_bf16_f32 v161, v215, v217
	v_exp_f32_e32 v195, v106
	v_exp_f32_e32 v197, v107
	v_exp_f32_e32 v219, v108
	v_exp_f32_e32 v221, v109
	v_mfma_f32_32x32x16_bf16 v[2:17], v[118:121], v[190:193], v[2:17]
	ds_read_b128 v[162:165], v210 offset:2560
	v_cvt_pk_bf16_f32 v146, v195, v197
	v_cvt_pk_bf16_f32 v147, v219, v221
	v_exp_f32_e32 v127, v110
	v_exp_f32_e32 v223, v111
	v_pk_add_f32 v[106:107], v[208:209], v[114:115]
	v_mfma_f32_32x32x16_bf16 v[18:33], v[122:125], v[190:193], v[18:33]
	v_add_f32_e64 v106, v214, v106
	v_add_f32_e64 v107, v215, v107
	v_exp_f32_e32 v129, v112
	v_pk_add_f32 v[106:107], v[216:217], v[106:107]
	ds_read_b128 v[166:169], v210 offset:6656
	v_pk_add_f32 v[234:235], v[194:195], v[234:235]
	v_exp_f32_e32 v171, v113
	v_pk_add_f32 v[106:107], v[196:197], v[106:107]
	v_cvt_pk_bf16_f32 v148, v127, v223
	v_pk_add_f32 v[234:235], v[218:219], v[234:235]
	v_cvt_pk_bf16_f32 v149, v129, v171
	v_pk_add_f32 v[106:107], v[220:221], v[106:107]
	v_pk_add_f32 v[234:235], v[126:127], v[234:235]
	v_pk_add_f32 v[106:107], v[222:223], v[106:107]
	v_pk_add_f32 v[234:235], v[128:129], v[234:235]
	v_pk_add_f32 v[178:179], v[170:171], v[106:107]
	s_add_i32 s27, s22, 1
	s_waitcnt vmcnt(0)
	s_and_b32 s28, s27, 3
	s_add_i32 s26, s26, 1
	s_cmpk_eq_i32 s26, 0x104
	s_mov_b32 s27, s25
	s_mov_b32 s25, s23
	s_mov_b32 s23, s22
	s_mov_b32 s22, s28
	s_waitcnt vmcnt(0) lgkmcnt(0)
	s_barrier
	s_cbranch_scc0 .LBB0_953
	v_add_f32_e32 v178, v178, v234
	v_add_f32_e32 v179, v179, v235
	ds_read_b128 v[66:69], v189 offset:12288
	ds_read_b128 v[70:73], v189 offset:12800
	v_mov_b32_e32 v0, v230
	s_waitcnt lgkmcnt(1)
	v_mfma_f32_32x32x16_bf16 v[34:49], v[66:69], v[150:153], v[34:49]
	s_waitcnt lgkmcnt(0)
	v_mfma_f32_32x32x16_bf16 v[50:65], v[70:73], v[150:153], v[50:65]
	v_mfma_f32_32x32x16_bf16 v[2:17], v[66:69], v[158:161], v[2:17]
	v_mfma_f32_32x32x16_bf16 v[18:33], v[70:73], v[158:161], v[18:33]
	ds_read_b128 v[68:71], v189 offset:14336
	ds_read_b128 v[72:75], v189 offset:14848
	v_mbcnt_lo_u32_b32 v76, -1, 0
	v_mbcnt_hi_u32_b32 v76, -1, v76
	v_mbcnt_lo_u32_b32 v77, -1, 0
	v_mbcnt_hi_u32_b32 v77, -1, v77
	global_load_dwordx2 v[66:67], v1, s[6:7]
	v_lshlrev_b32_e32 v77, 2, v77
	v_xor_b32_e32 v77, 0x80, v77
	v_lshlrev_b32_e32 v76, 2, v76
	ds_bpermute_b32 v77, v77, v179
	v_xor_b32_e32 v76, 0x80, v76
	ds_bpermute_b32 v76, v76, v178
	s_waitcnt lgkmcnt(3)
	v_mfma_f32_32x32x16_bf16 v[2:17], v[68:71], v[146:149], v[2:17]
	v_readfirstlane_b32 s21, v0
	s_ashr_i32 s21, s21, 1
	s_andn2_b32 s21, s21, 31
	s_cmpk_lt_i32 s21, 0x100
	s_waitcnt lgkmcnt(2)
	v_mfma_f32_32x32x16_bf16 v[18:33], v[72:75], v[146:149], v[18:33]
	v_mfma_f32_32x32x16_bf16 v[34:49], v[68:71], v[154:157], v[34:49]
	s_waitcnt lgkmcnt(1)
	v_add_f32_e32 v70, v179, v77
	v_mbcnt_lo_u32_b32 v68, -1, 0
	v_mbcnt_hi_u32_b32 v68, -1, v68
	v_rcp_f32_e32 v70, v70
	v_lshlrev_b32_e32 v69, 2, v68
	s_waitcnt lgkmcnt(0)
	v_add_f32_e32 v68, v178, v76
	v_rcp_f32_e32 v68, v68
	s_waitcnt vmcnt(0)
	v_mul_f32_e32 v66, v66, v70
	v_mfma_f32_32x32x16_bf16 v[50:65], v[72:75], v[154:157], v[50:65]
	v_mul_f32_e64 v2, v2, v66
	v_mul_f32_e64 v3, v3, v66
	v_mul_f32_e64 v18, v18, v66
	v_mul_f32_e64 v19, v19, v66
	v_mul_f32_e64 v4, v4, v66
	v_mul_f32_e64 v5, v5, v66
	v_pk_mul_f32 v[20:21], v[20:21], v[66:67] op_sel_hi:[1,0]
	v_pk_mul_f32 v[70:71], v[24:25], v[66:67] op_sel_hi:[1,0]
	v_pk_fma_f32 v[24:25], v[34:35], v[68:69], v[2:3] op_sel_hi:[1,0,1] neg_lo:[0,0,1] neg_hi:[0,0,1]
	v_pk_mul_f32 v[72:73], v[26:27], v[66:67] op_sel_hi:[1,0]
	s_nop 1
	v_pk_fma_f32 v[2:3], v[50:51], v[68:69], v[18:19] op_sel_hi:[1,0,1] neg_lo:[0,0,1] neg_hi:[0,0,1]
	v_pk_fma_f32 v[26:27], v[36:37], v[68:69], v[4:5] op_sel_hi:[1,0,1] neg_lo:[0,0,1] neg_hi:[0,0,1]
	v_pk_fma_f32 v[4:5], v[52:53], v[68:69], v[20:21] op_sel_hi:[1,0,1] neg_lo:[0,0,1] neg_hi:[0,0,1]
	v_pk_mul_f32 v[18:19], v[2:3], v[2:3]
	v_pk_mul_f32 v[6:7], v[6:7], v[66:67] op_sel_hi:[1,0]
	v_pk_mul_f32 v[22:23], v[22:23], v[66:67] op_sel_hi:[1,0]
	v_pk_mul_f32 v[36:37], v[4:5], v[4:5]
	v_pk_fma_f32 v[18:19], v[24:25], v[24:25], v[18:19]
	v_pk_mul_f32 v[74:75], v[28:29], v[66:67] op_sel_hi:[1,0]
	v_pk_fma_f32 v[28:29], v[38:39], v[68:69], v[6:7] op_sel_hi:[1,0,1] neg_lo:[0,0,1] neg_hi:[0,0,1]
	v_pk_fma_f32 v[6:7], v[54:55], v[68:69], v[22:23] op_sel_hi:[1,0,1] neg_lo:[0,0,1] neg_hi:[0,0,1]
	v_pk_fma_f32 v[36:37], v[26:27], v[26:27], v[36:37]
	v_add_f32_e32 v18, v18, v19
	v_pk_mul_f32 v[8:9], v[8:9], v[66:67] op_sel_hi:[1,0]
	v_pk_mul_f32 v[38:39], v[6:7], v[6:7]
	v_add_f32_e32 v18, v36, v18
	v_pk_mul_f32 v[76:77], v[30:31], v[66:67] op_sel_hi:[1,0]
	v_pk_fma_f32 v[30:31], v[40:41], v[68:69], v[8:9] op_sel_hi:[1,0,1] neg_lo:[0,0,1] neg_hi:[0,0,1]
	v_pk_fma_f32 v[8:9], v[56:57], v[68:69], v[70:71] op_sel_hi:[1,0,1] neg_lo:[0,0,1] neg_hi:[0,0,1]
	v_pk_fma_f32 v[38:39], v[28:29], v[28:29], v[38:39]
	v_add_f32_e32 v18, v37, v18
	v_pk_mul_f32 v[10:11], v[10:11], v[66:67] op_sel_hi:[1,0]
	v_pk_mul_f32 v[40:41], v[8:9], v[8:9]
	v_add_f32_e32 v18, v38, v18
	v_pk_mul_f32 v[78:79], v[32:33], v[66:67] op_sel_hi:[1,0]
	v_pk_fma_f32 v[32:33], v[42:43], v[68:69], v[10:11] op_sel_hi:[1,0,1] neg_lo:[0,0,1] neg_hi:[0,0,1]
	v_pk_fma_f32 v[10:11], v[58:59], v[68:69], v[72:73] op_sel_hi:[1,0,1] neg_lo:[0,0,1] neg_hi:[0,0,1]
	v_pk_fma_f32 v[40:41], v[30:31], v[30:31], v[40:41]
	v_add_f32_e32 v18, v39, v18
	v_pk_mul_f32 v[12:13], v[12:13], v[66:67] op_sel_hi:[1,0]
	v_pk_mul_f32 v[42:43], v[10:11], v[10:11]
	v_add_f32_e32 v18, v40, v18
	v_pk_fma_f32 v[34:35], v[44:45], v[68:69], v[12:13] op_sel_hi:[1,0,1] neg_lo:[0,0,1] neg_hi:[0,0,1]
	v_pk_fma_f32 v[12:13], v[60:61], v[68:69], v[74:75] op_sel_hi:[1,0,1] neg_lo:[0,0,1] neg_hi:[0,0,1]
	v_pk_fma_f32 v[42:43], v[32:33], v[32:33], v[42:43]
	v_add_f32_e32 v18, v41, v18
	v_pk_mul_f32 v[14:15], v[14:15], v[66:67] op_sel_hi:[1,0]
	v_pk_mul_f32 v[44:45], v[12:13], v[12:13]
	v_add_f32_e32 v18, v42, v18
	v_pk_fma_f32 v[20:21], v[46:47], v[68:69], v[14:15] op_sel_hi:[1,0,1] neg_lo:[0,0,1] neg_hi:[0,0,1]
	v_pk_fma_f32 v[14:15], v[62:63], v[68:69], v[76:77] op_sel_hi:[1,0,1] neg_lo:[0,0,1] neg_hi:[0,0,1]
	v_pk_fma_f32 v[44:45], v[34:35], v[34:35], v[44:45]
	v_add_f32_e32 v18, v43, v18
	v_pk_mul_f32 v[16:17], v[16:17], v[66:67] op_sel_hi:[1,0]
	v_pk_mul_f32 v[46:47], v[14:15], v[14:15]
	v_add_f32_e32 v18, v44, v18
	v_pk_fma_f32 v[22:23], v[48:49], v[68:69], v[16:17] op_sel_hi:[1,0,1] neg_lo:[0,0,1] neg_hi:[0,0,1]
	v_pk_fma_f32 v[16:17], v[64:65], v[68:69], v[78:79] op_sel_hi:[1,0,1] neg_lo:[0,0,1] neg_hi:[0,0,1]
	v_pk_fma_f32 v[46:47], v[20:21], v[20:21], v[46:47]
	v_add_f32_e32 v18, v45, v18
	v_pk_mul_f32 v[48:49], v[16:17], v[16:17]
	v_add_f32_e32 v18, v46, v18
	v_pk_fma_f32 v[48:49], v[22:23], v[22:23], v[48:49]
	v_add_f32_e32 v18, v47, v18
	v_add_f32_e32 v18, v48, v18
	v_add_f32_e32 v36, v49, v18
	v_xor_b32_e32 v18, 0x80, v69
	ds_bpermute_b32 v37, v18, v36
	s_cbranch_scc0 .LBB0_951
	s_waitcnt lgkmcnt(0)
	v_add_f32_e32 v36, v36, v37
	v_fmamk_f32 v36, v36, 0x3c800000, v224
	v_cmp_gt_f32_e32 vcc, s31, v36
	v_mul_f32_e32 v37, 0x4b800000, v36
	v_and_or_b32 v18, v0, 31, s21
	v_cndmask_b32_e32 v36, v36, v37, vcc
	v_rsq_f32_e32 v36, v36
	v_lshrrev_b32_e32 v0, 3, v0
	v_and_b32_e32 v0, 4, v0
	v_lshlrev_b32_e32 v41, 2, v0
	v_mul_f32_e32 v37, 0x45800000, v36
	v_cndmask_b32_e32 v36, v36, v37, vcc
	v_mul_f32_e32 v40, v67, v36
	global_load_dwordx4 v[36:39], v41, s[8:9] offset:128
	s_lshl_b64 s[10:11], s[10:11], 11
	s_add_u32 s10, s2, s10
	s_addc_u32 s11, s3, s11
	s_lshl_b32 s20, s20, 1
	s_add_u32 s10, s10, s20
	v_ashrrev_i32_e32 v19, 31, v18
	s_addc_u32 s11, s11, 0
	v_lshlrev_b64 v[18:19], 11, v[18:19]
	v_lshl_add_u64 v[18:19], s[10:11], 0, v[18:19]
	v_lshlrev_b32_e32 v0, 1, v0
	v_lshl_add_u64 v[18:19], v[18:19], 0, v[0:1]
	s_waitcnt vmcnt(0)
	v_pk_mul_f32 v[36:37], v[40:41], v[36:37] op_sel_hi:[0,1]
	v_pk_mul_f32 v[2:3], v[2:3], v[36:37]
	v_pk_mul_f32 v[36:37], v[40:41], v[38:39] op_sel_hi:[0,1]
	v_pk_mul_f32 v[4:5], v[4:5], v[36:37]
	global_load_dwordx4 v[36:39], v41, s[8:9] offset:160
	v_cvt_pk_bf16_f32 v2, v2, v3
	v_cvt_pk_bf16_f32 v3, v4, v5
	s_waitcnt vmcnt(0)
	v_pk_mul_f32 v[36:37], v[40:41], v[36:37] op_sel_hi:[0,1]
	v_pk_mul_f32 v[6:7], v[6:7], v[36:37]
	v_pk_mul_f32 v[36:37], v[40:41], v[38:39] op_sel_hi:[0,1]
	v_pk_mul_f32 v[8:9], v[8:9], v[36:37]
	global_load_dwordx4 v[36:39], v41, s[8:9] offset:192
	v_cvt_pk_bf16_f32 v4, v6, v7
	v_cvt_pk_bf16_f32 v5, v8, v9
	s_waitcnt vmcnt(0)
	v_pk_mul_f32 v[36:37], v[40:41], v[36:37] op_sel_hi:[0,1]
	v_pk_mul_f32 v[10:11], v[10:11], v[36:37]
	v_pk_mul_f32 v[36:37], v[40:41], v[38:39] op_sel_hi:[0,1]
	v_pk_mul_f32 v[12:13], v[12:13], v[36:37]
	global_load_dwordx4 v[36:39], v41, s[8:9] offset:224
	s_waitcnt vmcnt(0)
	v_pk_mul_f32 v[36:37], v[40:41], v[36:37] op_sel_hi:[0,1]
	v_pk_mul_f32 v[14:15], v[14:15], v[36:37]
	v_pk_mul_f32 v[36:37], v[40:41], v[38:39] op_sel_hi:[0,1]
	v_pk_mul_f32 v[16:17], v[16:17], v[36:37]
	global_load_dwordx4 v[36:39], v41, s[8:9]
	s_waitcnt vmcnt(0)
	v_pk_mul_f32 v[36:37], v[40:41], v[36:37] op_sel_hi:[0,1]
	v_pk_mul_f32 v[24:25], v[24:25], v[36:37]
	v_pk_mul_f32 v[36:37], v[40:41], v[38:39] op_sel_hi:[0,1]
	v_pk_mul_f32 v[26:27], v[26:27], v[36:37]
	global_load_dwordx4 v[36:39], v41, s[8:9] offset:32
	v_cvt_pk_bf16_f32 v24, v24, v25
	v_cvt_pk_bf16_f32 v25, v26, v27
	s_waitcnt vmcnt(0)
	v_pk_mul_f32 v[36:37], v[40:41], v[36:37] op_sel_hi:[0,1]
	v_pk_mul_f32 v[28:29], v[28:29], v[36:37]
	v_pk_mul_f32 v[36:37], v[40:41], v[38:39] op_sel_hi:[0,1]
	v_pk_mul_f32 v[30:31], v[30:31], v[36:37]
	global_load_dwordx4 v[36:39], v41, s[8:9] offset:64
	s_waitcnt vmcnt(0)
	v_pk_mul_f32 v[36:37], v[40:41], v[36:37] op_sel_hi:[0,1]
	v_pk_mul_f32 v[32:33], v[32:33], v[36:37]
	v_pk_mul_f32 v[36:37], v[40:41], v[38:39] op_sel_hi:[0,1]
	v_pk_mul_f32 v[34:35], v[34:35], v[36:37]
	global_load_dwordx4 v[36:39], v41, s[8:9] offset:96
	s_nop 0
	global_store_dwordx2 v[18:19], v[24:25], off offset:1024
	global_store_dwordx2 v[18:19], v[2:3], off offset:1088
	v_cvt_pk_bf16_f32 v2, v28, v29
	v_cvt_pk_bf16_f32 v3, v30, v31
	global_store_dwordx2 v[18:19], v[2:3], off offset:1040
	global_store_dwordx2 v[18:19], v[4:5], off offset:1104
	v_cvt_pk_bf16_f32 v2, v32, v33
	v_cvt_pk_bf16_f32 v3, v34, v35
	v_cvt_pk_bf16_f32 v4, v10, v11
	v_cvt_pk_bf16_f32 v5, v12, v13
	global_store_dwordx2 v[18:19], v[2:3], off offset:1056
	global_store_dwordx2 v[18:19], v[4:5], off offset:1120
	v_cvt_pk_bf16_f32 v4, v14, v15
	v_cvt_pk_bf16_f32 v5, v16, v17
	s_waitcnt vmcnt(6)
	v_pk_mul_f32 v[36:37], v[40:41], v[36:37] op_sel_hi:[0,1]
	v_pk_mul_f32 v[20:21], v[20:21], v[36:37]
	v_pk_mul_f32 v[36:37], v[40:41], v[38:39] op_sel_hi:[0,1]
	v_pk_mul_f32 v[22:23], v[22:23], v[36:37]
	v_cvt_pk_bf16_f32 v2, v20, v21
	v_cvt_pk_bf16_f32 v3, v22, v23
	global_store_dwordx2 v[18:19], v[2:3], off offset:1072
	global_store_dwordx2 v[18:19], v[4:5], off offset:1136
	s_branch .LBB0_951

.LBB0_966:
	s_ashr_i32 s16, s14, 7
	s_ashr_i32 s17, s16, 31
	s_lshl_b32 s15, s14, 8
	s_lshl_b64 s[6:7], s[16:17], 14
	s_and_b32 s15, s15, 0x3f00
	s_or_b32 s6, s6, s15
	s_bfe_u32 s19, s14, 0x10006
	s_lshl_b64 s[20:21], s[6:7], 9
	s_add_u32 s17, s8, s20
	s_addc_u32 s21, s9, s21
	s_lshl_b32 s15, s19, 7
	s_lshl_b32 s20, s19, 8
	s_add_u32 s20, s17, s20
	s_addc_u32 s21, s21, 0
	s_lshl_b32 s16, s16, 1
	s_or_b32 s16, s16, s19
	s_mul_hi_i32 s17, s16, 0x208000
	s_mul_i32 s16, s16, 0x208000
	s_add_u32 s19, s10, s16
	s_addc_u32 s22, s11, s17
	v_mov_b32_e32 v4, v230
	s_add_u32 s23, s12, s16
	s_addc_u32 s17, s13, s17
	v_readfirstlane_b32 s16, v4
	v_and_b32_e32 v14, 31, v4
	s_ashr_i32 s16, s16, 6
	s_cmp_lt_i32 s16, 8
	v_lshl_or_b32 v0, s16, 5, v14
	v_ashrrev_i32_e32 v2, 31, v0
	s_cselect_b64 vcc, -1, 0
	v_cndmask_b32_e32 v3, 0, v2, vcc
	v_cndmask_b32_e32 v2, v14, v0, vcc
	v_bfe_u32 v5, v4, 5, 1
	v_lshlrev_b64 v[2:3], 9, v[2:3]
	v_lshl_add_u64 v[2:3], s[20:21], 0, v[2:3]
	v_lshlrev_b32_e32 v0, 4, v5
	v_lshl_add_u64 v[2:3], v[2:3], 0, v[0:1]
	global_load_dwordx4 v[130:133], v[2:3], off
	global_load_dwordx4 v[134:137], v[2:3], off offset:128
	global_load_dwordx4 v[138:141], v[2:3], off offset:32
	global_load_dwordx4 v[142:145], v[2:3], off offset:160
	global_load_dwordx4 v[146:149], v[2:3], off offset:64
	global_load_dwordx4 v[150:153], v[2:3], off offset:192
	global_load_dwordx4 v[154:157], v[2:3], off offset:96
	global_load_dwordx4 v[158:161], v[2:3], off offset:224
	s_lshl_b32 s25, s16, 10
	s_ashr_i32 s26, s25, 31
	s_add_u32 s20, s19, s25
	v_and_b32_e32 v0, 63, v4
	s_addc_u32 s21, s22, s26
	s_add_i32 s16, s25, 0
	v_lshlrev_b32_e32 v0, 4, v0
	s_add_u32 s22, s23, s25
	s_mov_b32 m0, s16
	s_mov_b32 s56, s20
	s_mov_b32 s57, s21
	v_lshl_add_u64 v[194:195], s[20:21], 0, v[0:1]
	global_load_lds_dwordx4 v0, s[20:21]
	s_addc_u32 s23, s17, s26
	s_add_i32 m0, s16, 0x2000
	s_mov_b64 s[20:21], 0x2000
	s_mov_b32 s58, s22
	s_mov_b32 s59, s23
	v_lshl_add_u64 v[196:197], s[22:23], 0, v[0:1]
	global_load_lds_dwordx4 v0, s[22:23]
	v_lshl_add_u64 v[2:3], v[194:195], 0, s[20:21]
	s_add_i32 m0, s16, 0x4000
	v_and_b32_e32 v6, 19, v4
	global_load_lds_dwordx4 v[2:3], off
	v_lshl_add_u64 v[2:3], v[196:197], 0, s[20:21]
	s_add_i32 m0, s16, 0x6000
	v_lshlrev_b32_e32 v7, 1, v4
	global_load_lds_dwordx4 v[2:3], off
	v_lshrrev_b32_e32 v4, 1, v4
	v_lshlrev_b32_e32 v15, 10, v5
	v_and_b32_e32 v5, 8, v7
	v_and_b32_e32 v4, 4, v4
	v_or3_b32 v4, v6, v5, v4
	v_lshl_or_b32 v214, v4, 4, v15
	v_mov_b32_e32 v162, v1
	v_add_u32_e32 v215, 0, v214
	s_waitcnt vmcnt(0)
	s_waitcnt vmcnt(0) lgkmcnt(0)
	s_barrier
	ds_read_b128 v[2:5], v215
	ds_read_b128 v[98:101], v215 offset:512
	v_lshl_or_b32 v0, v14, 4, v15
	s_mov_b32 s17, 1
	s_mov_b32 s22, 0
	s_mov_b32 s19, 2
	s_mov_b32 s20, 0
	s_mov_b32 s21, 0
	v_add_u32_e32 v231, 0, v0
	v_mov_b32_e32 v163, v162
	v_mov_b32_e32 v164, v162
	v_mov_b32_e32 v165, v162
	v_mov_b32_e32 v166, v162
	v_mov_b32_e32 v167, v162
	v_mov_b32_e32 v168, v162
	v_mov_b32_e32 v169, v162
	s_waitcnt lgkmcnt(1)
	v_mfma_f32_32x32x16_bf16 v[82:97], v[2:5], v[130:133], 0
	v_mov_b32_e32 v174, v162
	v_mov_b32_e32 v175, v162
	v_mov_b32_e32 v176, v162
	v_mov_b32_e32 v177, v162
	v_mov_b32_e32 v170, v162
	v_mov_b32_e32 v171, v162
	v_mov_b32_e32 v172, v162
	v_mfma_f32_32x32x16_bf16 v[66:81], v[2:5], v[134:137], 0
	ds_read_b128 v[2:5], v215 offset:2048
	ds_read_b128 v[178:181], v215 offset:2560
	ds_read_b128 v[6:9], v215 offset:4096
	ds_read_b128 v[10:13], v215 offset:6144
	v_mov_b32_e32 v173, v162
	s_waitcnt lgkmcnt(3)
	v_mfma_f32_32x32x16_bf16 v[82:97], v[2:5], v[138:141], v[82:97]
	v_mfma_f32_32x32x16_bf16 v[66:81], v[2:5], v[142:145], v[66:81]
	v_mov_b32_e32 v2, 0
	v_mov_b32_e32 v3, v2
	v_mov_b32_e32 v4, v2
	v_mov_b32_e32 v5, v2
	v_mov_b32_e32 v14, v2
	v_mov_b32_e32 v15, v2
	v_mov_b32_e32 v16, v2
	s_waitcnt lgkmcnt(1)
	v_mfma_f32_32x32x16_bf16 v[82:97], v[6:9], v[146:149], v[82:97]
	v_mov_b32_e32 v17, v2
	v_mov_b32_e32 v18, v2
	v_mov_b32_e32 v19, v2
	v_mov_b32_e32 v20, v2
	v_mov_b32_e32 v21, v2
	v_mov_b32_e32 v22, v2
	v_mov_b32_e32 v23, v2
	v_mfma_f32_32x32x16_bf16 v[66:81], v[6:9], v[150:153], v[66:81]
	v_mov_b32_e32 v6, v2
	v_mov_b32_e32 v7, v2
	v_mov_b32_e32 v8, v2
	v_mov_b32_e32 v9, v2
	v_mov_b32_e32 v24, v2
	v_mov_b32_e32 v25, v2
	v_mov_b32_e32 v26, v2
	s_waitcnt lgkmcnt(0)
	v_mfma_f32_32x32x16_bf16 v[82:97], v[10:13], v[154:157], v[82:97]
	v_mov_b32_e32 v27, v2
	v_mov_b32_e32 v28, v2
	v_mov_b32_e32 v29, v2
	v_mov_b32_e32 v30, v2
	v_mov_b32_e32 v31, v2
	v_mov_b32_e32 v32, v2
	v_mov_b32_e32 v33, v2
	v_mfma_f32_32x32x16_bf16 v[66:81], v[10:13], v[158:161], v[66:81]
	v_mov_b32_e32 v10, v2
	v_mov_b32_e32 v11, v2
	v_mov_b32_e32 v12, v2
	v_mov_b32_e32 v13, v2
	v_mov_b32_e32 v50, v2
	v_mov_b32_e32 v51, v2
	v_mov_b32_e32 v52, v2
	v_mov_b32_e32 v53, v2
	v_mov_b32_e32 v54, v2
	v_mov_b32_e32 v55, v2
	v_mov_b32_e32 v56, v2
	v_mov_b32_e32 v57, v2
	v_mov_b32_e32 v58, v2
	v_mov_b32_e32 v59, v2
	v_mov_b32_e32 v60, v2
	v_mov_b32_e32 v61, v2
	v_mov_b32_e32 v62, v2
	v_mov_b32_e32 v63, v2
	v_mov_b32_e32 v64, v2
	v_mov_b32_e32 v65, v2
	v_mov_b32_e32 v34, v2
	v_mov_b32_e32 v35, v2
	v_mov_b32_e32 v36, v2
	v_mov_b32_e32 v37, v2
	v_mov_b32_e32 v38, v2
	v_mov_b32_e32 v39, v2
	v_mov_b32_e32 v40, v2
	v_mov_b32_e32 v41, v2
	v_mov_b32_e32 v42, v2
	v_mov_b32_e32 v43, v2
	v_mov_b32_e32 v44, v2
	v_mov_b32_e32 v45, v2
	v_mov_b32_e32 v46, v2
	v_mov_b32_e32 v47, v2
	v_mov_b32_e32 v48, v2
	v_mov_b32_e32 v49, v2
	v_mov_b32_e32 v186, v2
	v_mov_b32_e32 v187, v2
	v_mov_b32_e32 v233, v186
	v_mov_b32_e32 v227, v187
	v_mbcnt_lo_u32_b32 v194, -1, 0
	v_mbcnt_hi_u32_b32 v194, -1, v194
	v_lshlrev_b32_e32 v194, 4, v194
.LBB0_967:
	v_mfma_f32_32x32x16_bf16 v[114:129], v[98:101], v[130:133], 0
	s_min_i32 s23, s21, 0x101
	s_lshl_b32 s23, s23, 13
	s_add_i32 s88, s23, 0x4000
	s_lshl_b32 s23, s19, 14
	s_add_i32 s23, s16, s23
	s_add_u32 s60, s56, s88
	s_addc_u32 s61, s57, s89
	s_mov_b32 m0, s23
	v_lshl_add_u32 v211, s17, 14, v215
	global_load_lds_dwordx4 v194, s[60:61]
	s_add_u32 s62, s58, s88
	s_addc_u32 s63, s59, s89
	s_add_i32 m0, s23, 0x2000
	s_lshl_b32 s23, s20, 14
	global_load_lds_dwordx4 v194, s[62:63]
	s_add_i32 s23, s23, 0
	v_add_u32_e32 v183, s23, v214
	ds_read_b128 v[188:191], v183 offset:4608
	v_add_u32_e32 v232, s23, v0
	v_lshl_add_u32 v192, s22, 14, v231
	v_exp_f32_e32 v216, v82
	v_exp_f32_e32 v218, v83
	v_mfma_f32_32x32x16_bf16 v[98:113], v[98:101], v[134:137], 0
	v_cvt_pk_bf16_f32 v182, v216, v218
	v_add_f32_e32 v233, v216, v233
	v_add_f32_e32 v233, v218, v233
	v_exp_f32_e32 v220, v84
	v_exp_f32_e32 v222, v85
	v_mfma_f32_32x32x16_bf16 v[114:129], v[178:181], v[138:141], v[114:129]
	ds_read_b128 v[82:85], v183 offset:6656
	v_cvt_pk_bf16_f32 v183, v220, v222
	v_add_f32_e32 v233, v220, v233
	v_add_f32_e32 v233, v222, v233
	v_exp_f32_e32 v224, v86
	v_exp_f32_e32 v238, v87
	v_mfma_f32_32x32x16_bf16 v[98:113], v[178:181], v[142:145], v[98:113]
	v_cvt_pk_bf16_f32 v184, v224, v238
	v_add_f32_e32 v233, v224, v233
	v_add_f32_e32 v233, v238, v233
	v_exp_f32_e32 v240, v88
	v_exp_f32_e32 v242, v89
	s_waitcnt lgkmcnt(1)
	v_mfma_f32_32x32x16_bf16 v[114:129], v[188:191], v[146:149], v[114:129]
	ds_read_b128 v[86:89], v192 offset:12288
	v_cvt_pk_bf16_f32 v185, v240, v242
	v_add_f32_e32 v233, v240, v233
	v_add_f32_e32 v233, v242, v233
	v_exp_f32_e32 v244, v90
	v_exp_f32_e32 v246, v91
	v_mfma_f32_32x32x16_bf16 v[98:113], v[188:191], v[150:153], v[98:113]
	ds_read_b128 v[234:237], v192 offset:12800
	v_cvt_pk_bf16_f32 v178, v244, v246
	v_add_f32_e32 v233, v244, v233
	v_add_f32_e32 v233, v246, v233
	v_exp_f32_e32 v200, v92
	v_exp_f32_e32 v198, v93
	s_waitcnt lgkmcnt(2)
	v_mfma_f32_32x32x16_bf16 v[114:129], v[82:85], v[154:157], v[114:129]
	s_nop 0
	v_cvt_pk_bf16_f32 v179, v200, v198
	v_add_f32_e32 v233, v200, v233
	v_add_f32_e32 v233, v198, v233
	v_exp_f32_e32 v204, v94
	v_exp_f32_e32 v202, v95
	v_mfma_f32_32x32x16_bf16 v[98:113], v[82:85], v[158:161], v[98:113]
	v_cvt_pk_bf16_f32 v180, v204, v202
	v_add_f32_e32 v233, v204, v233
	v_add_f32_e32 v233, v202, v233
	v_exp_f32_e32 v208, v96
	v_exp_f32_e32 v206, v97
	s_waitcnt lgkmcnt(1)
	v_mfma_f32_32x32x16_bf16 v[2:17], v[86:89], v[162:165], v[2:17]
	ds_read_b128 v[82:85], v192 offset:14336
	v_cvt_pk_bf16_f32 v181, v208, v206
	v_add_f32_e32 v233, v208, v233
	v_add_f32_e32 v233, v206, v233
	v_exp_f32_e32 v217, v66
	v_exp_f32_e32 v219, v67
	s_waitcnt lgkmcnt(1)
	v_mfma_f32_32x32x16_bf16 v[18:33], v[234:237], v[162:165], v[18:33]
	ds_read_b128 v[90:93], v192 offset:14848
	v_cvt_pk_bf16_f32 v190, v217, v219
	v_add_f32_e32 v227, v217, v227
	v_add_f32_e32 v227, v219, v227
	v_exp_f32_e32 v221, v68
	v_exp_f32_e32 v223, v69
	v_mfma_f32_32x32x16_bf16 v[34:49], v[86:89], v[174:177], v[34:49]
	v_cvt_pk_bf16_f32 v191, v221, v223
	v_add_f32_e32 v227, v221, v227
	v_add_f32_e32 v227, v223, v227
	v_exp_f32_e32 v225, v70
	v_exp_f32_e32 v239, v71
	v_mfma_f32_32x32x16_bf16 v[50:65], v[234:237], v[174:177], v[50:65]
	v_cvt_pk_bf16_f32 v192, v225, v239
	v_add_f32_e32 v227, v225, v227
	v_add_f32_e32 v227, v239, v227
	v_exp_f32_e32 v241, v72
	v_exp_f32_e32 v243, v73
	s_waitcnt lgkmcnt(1)
	v_mfma_f32_32x32x16_bf16 v[2:17], v[82:85], v[166:169], v[2:17]
	ds_read_b128 v[66:69], v211
	v_cvt_pk_bf16_f32 v193, v241, v243
	v_add_f32_e32 v227, v241, v227
	v_add_f32_e32 v227, v243, v227
	v_exp_f32_e32 v245, v74
	v_exp_f32_e32 v247, v75
	s_waitcnt lgkmcnt(1)
	v_mfma_f32_32x32x16_bf16 v[18:33], v[90:93], v[166:169], v[18:33]
	v_cvt_pk_bf16_f32 v186, v245, v247
	v_add_f32_e32 v227, v245, v227
	v_add_f32_e32 v227, v247, v227
	v_exp_f32_e32 v201, v76
	v_exp_f32_e32 v199, v77
	v_mfma_f32_32x32x16_bf16 v[34:49], v[82:85], v[170:173], v[34:49]
	ds_read_b128 v[164:167], v211 offset:2048
	v_cvt_pk_bf16_f32 v187, v201, v199
	v_add_f32_e32 v227, v201, v227
	v_add_f32_e32 v227, v199, v227
	v_exp_f32_e32 v205, v78
	v_exp_f32_e32 v203, v79
	v_mfma_f32_32x32x16_bf16 v[50:65], v[90:93], v[170:173], v[50:65]
	v_exp_f32_e32 v209, v80
	v_exp_f32_e32 v207, v81
	v_cvt_pk_bf16_f32 v188, v205, v203
	v_add_f32_e32 v227, v205, v227
	v_add_f32_e32 v227, v203, v227
	v_cvt_pk_bf16_f32 v189, v209, v207
	v_add_f32_e32 v227, v209, v227
	v_add_f32_e32 v227, v207, v227
	s_waitcnt lgkmcnt(1)
	v_mfma_f32_32x32x16_bf16 v[82:97], v[66:69], v[130:133], 0
	ds_read_b128 v[168:171], v211 offset:4096
	v_exp_f32_e32 v172, v114
	v_exp_f32_e32 v216, v115
	v_mfma_f32_32x32x16_bf16 v[66:81], v[66:69], v[134:137], 0
	v_cvt_pk_bf16_f32 v162, v172, v216
	v_add_f32_e32 v233, v172, v233
	v_add_f32_e32 v233, v216, v233
	v_exp_f32_e32 v218, v116
	v_exp_f32_e32 v220, v117
	s_waitcnt lgkmcnt(1)
	v_mfma_f32_32x32x16_bf16 v[82:97], v[164:167], v[138:141], v[82:97]
	ds_read_b128 v[114:117], v211 offset:6144
	v_cvt_pk_bf16_f32 v163, v218, v220
	v_add_f32_e32 v233, v218, v233
	v_add_f32_e32 v233, v220, v233
	v_exp_f32_e32 v222, v118
	v_exp_f32_e32 v224, v119
	v_mfma_f32_32x32x16_bf16 v[66:81], v[164:167], v[142:145], v[66:81]
	v_cvt_pk_bf16_f32 v164, v222, v224
	v_add_f32_e32 v233, v222, v233
	v_add_f32_e32 v233, v224, v233
	v_exp_f32_e32 v238, v120
	v_exp_f32_e32 v240, v121
	s_waitcnt lgkmcnt(1)
	v_mfma_f32_32x32x16_bf16 v[82:97], v[168:171], v[146:149], v[82:97]
	ds_read_b128 v[118:121], v232 offset:8192
	v_cvt_pk_bf16_f32 v165, v238, v240
	v_add_f32_e32 v233, v238, v233
	v_add_f32_e32 v233, v240, v233
	v_exp_f32_e32 v242, v122
	v_exp_f32_e32 v244, v123
	v_mfma_f32_32x32x16_bf16 v[66:81], v[168:171], v[150:153], v[66:81]
	ds_read_b128 v[234:237], v232 offset:8704
	v_cvt_pk_bf16_f32 v166, v242, v244
	v_add_f32_e32 v233, v242, v233
	v_add_f32_e32 v233, v244, v233
	v_exp_f32_e32 v246, v124
	v_exp_f32_e32 v248, v125
	s_waitcnt lgkmcnt(2)
	v_mfma_f32_32x32x16_bf16 v[82:97], v[114:117], v[154:157], v[82:97]
	v_cvt_pk_bf16_f32 v167, v246, v248
	v_add_f32_e32 v233, v246, v233
	v_add_f32_e32 v233, v248, v233
	v_exp_f32_e32 v126, v126
	v_exp_f32_e32 v212, v127
	v_mfma_f32_32x32x16_bf16 v[66:81], v[114:117], v[158:161], v[66:81]
	v_cvt_pk_bf16_f32 v168, v126, v212
	v_add_f32_e32 v233, v126, v233
	v_add_f32_e32 v233, v212, v233
	v_exp_f32_e32 v128, v128
	v_exp_f32_e32 v210, v129
	s_waitcnt lgkmcnt(1)
	v_mfma_f32_32x32x16_bf16 v[2:17], v[118:121], v[182:185], v[2:17]
	ds_read_b128 v[114:117], v232 offset:10240
	v_exp_f32_e32 v173, v98
	v_cvt_pk_bf16_f32 v169, v128, v210
	v_add_f32_e32 v233, v128, v233
	v_add_f32_e32 v233, v210, v233
	v_exp_f32_e32 v217, v99
	s_waitcnt lgkmcnt(1)
	v_mfma_f32_32x32x16_bf16 v[18:33], v[234:237], v[182:185], v[18:33]
	ds_read_b128 v[122:125], v232 offset:10752
	v_cvt_pk_bf16_f32 v174, v173, v217
	v_add_f32_e32 v227, v173, v227
	v_add_f32_e32 v227, v217, v227
	v_exp_f32_e32 v219, v100
	v_exp_f32_e32 v221, v101
	v_mfma_f32_32x32x16_bf16 v[34:49], v[118:121], v[190:193], v[34:49]
	v_cvt_pk_bf16_f32 v175, v219, v221
	v_add_f32_e32 v227, v219, v227
	v_add_f32_e32 v227, v221, v227
	v_exp_f32_e32 v223, v102
	v_exp_f32_e32 v225, v103
	v_mfma_f32_32x32x16_bf16 v[50:65], v[234:237], v[190:193], v[50:65]
	v_cvt_pk_bf16_f32 v176, v223, v225
	v_add_f32_e32 v227, v223, v227
	v_add_f32_e32 v227, v225, v227
	v_exp_f32_e32 v239, v104
	v_exp_f32_e32 v241, v105
	s_waitcnt lgkmcnt(1)
	v_mfma_f32_32x32x16_bf16 v[2:17], v[114:117], v[178:181], v[2:17]
	ds_read_b128 v[98:101], v211 offset:512
	v_cvt_pk_bf16_f32 v177, v239, v241
	v_add_f32_e32 v227, v239, v227
	v_add_f32_e32 v227, v241, v227
	v_exp_f32_e32 v243, v106
	v_exp_f32_e32 v245, v107
	s_waitcnt lgkmcnt(1)
	v_mfma_f32_32x32x16_bf16 v[18:33], v[122:125], v[178:181], v[18:33]
	v_cvt_pk_bf16_f32 v170, v243, v245
	v_add_f32_e32 v227, v243, v227
	v_add_f32_e32 v227, v245, v227
	v_exp_f32_e32 v247, v108
	v_exp_f32_e32 v249, v109
	v_mfma_f32_32x32x16_bf16 v[34:49], v[114:117], v[186:189], v[34:49]
	ds_read_b128 v[178:181], v211 offset:2560
	v_cvt_pk_bf16_f32 v171, v247, v249
	v_add_f32_e32 v227, v247, v227
	v_add_f32_e32 v227, v249, v227
	v_exp_f32_e32 v127, v110
	v_exp_f32_e32 v213, v111
	v_mfma_f32_32x32x16_bf16 v[50:65], v[122:125], v[186:189], v[50:65]
	v_exp_f32_e32 v129, v112
	v_exp_f32_e32 v211, v113
	v_cvt_pk_bf16_f32 v172, v127, v213
	v_add_f32_e32 v227, v127, v227
	v_add_f32_e32 v227, v213, v227
	v_cvt_pk_bf16_f32 v173, v129, v211
	v_add_f32_e32 v227, v129, v227
	v_add_f32_e32 v227, v211, v227
	s_add_i32 s22, s19, 1
	s_waitcnt vmcnt(0)
	s_and_b32 s23, s22, 3
	s_add_i32 s21, s21, 1
	s_cmpk_eq_i32 s21, 0x104
	s_mov_b32 s22, s20
	s_mov_b32 s20, s17
	s_mov_b32 s17, s19
	s_mov_b32 s19, s23
	s_waitcnt vmcnt(0) lgkmcnt(0)
	s_barrier
	s_cbranch_scc0 .LBB0_967
	v_mov_b32_e32 v186, v233
	v_mov_b32_e32 v187, v227
	v_mov_b32_e32 v227, 0x7c
	ds_read_b128 v[66:69], v232 offset:12288
	ds_read_b128 v[70:73], v232 offset:12800
	v_mov_b32_e32 v0, v230
	s_waitcnt lgkmcnt(1)
	v_mfma_f32_32x32x16_bf16 v[2:17], v[66:69], v[162:165], v[2:17]
	s_waitcnt lgkmcnt(0)
	v_mfma_f32_32x32x16_bf16 v[18:33], v[70:73], v[162:165], v[18:33]
	v_mfma_f32_32x32x16_bf16 v[34:49], v[66:69], v[174:177], v[34:49]
	v_mfma_f32_32x32x16_bf16 v[50:65], v[70:73], v[174:177], v[50:65]
	ds_read_b128 v[66:69], v232 offset:14336
	ds_read_b128 v[70:73], v232 offset:14848
	s_nop 0
	v_readfirstlane_b32 s16, v0
	s_ashr_i32 s16, s16, 1
	s_andn2_b32 s16, s16, 31
	s_cmpk_lt_i32 s16, 0x100
	s_waitcnt lgkmcnt(1)
	v_mfma_f32_32x32x16_bf16 v[2:17], v[66:69], v[166:169], v[2:17]
	s_waitcnt lgkmcnt(0)
	v_mfma_f32_32x32x16_bf16 v[18:33], v[70:73], v[166:169], v[18:33]
	v_mfma_f32_32x32x16_bf16 v[34:49], v[66:69], v[170:173], v[34:49]
	v_mbcnt_lo_u32_b32 v66, -1, 0
	v_mbcnt_hi_u32_b32 v66, -1, v66
	v_mbcnt_lo_u32_b32 v67, -1, 0
	v_mbcnt_hi_u32_b32 v67, -1, v67
	s_nop 0
	v_lshlrev_b32_e32 v66, 2, v66
	v_lshlrev_b32_e32 v67, 2, v67
	v_xor_b32_e32 v66, 0x80, v66
	v_xor_b32_e32 v67, 0x80, v67
	v_mfma_f32_32x32x16_bf16 v[50:65], v[70:73], v[170:173], v[50:65]
	ds_bpermute_b32 v66, v66, v186
	ds_bpermute_b32 v67, v67, v187
	s_cbranch_scc0 .LBB0_965
	s_lshl_b64 s[6:7], s[6:7], 11
	s_waitcnt lgkmcnt(1)
	v_add_f32_e32 v66, v186, v66
	s_add_u32 s6, s2, s6
	v_rcp_f32_e32 v66, v66
	s_addc_u32 s7, s3, s7
	s_lshl_b32 s15, s15, 1
	v_and_or_b32 v68, v0, 31, s16
	s_add_u32 s6, s6, s15
	v_ashrrev_i32_e32 v69, 31, v68
	s_addc_u32 s7, s7, 0
	s_waitcnt lgkmcnt(0)
	v_add_f32_e32 v67, v187, v67
	v_lshlrev_b64 v[68:69], 11, v[68:69]
	v_lshrrev_b32_e32 v0, 2, v0
	v_rcp_f32_e32 v70, v67
	v_lshl_add_u64 v[68:69], s[6:7], 0, v[68:69]
	v_pk_mul_f32 v[2:3], v[2:3], v[66:67] op_sel_hi:[1,0]
	v_pk_mul_f32 v[4:5], v[4:5], v[66:67] op_sel_hi:[1,0]
	v_and_b32_e32 v0, 8, v0
	v_pk_mul_f32 v[18:19], v[18:19], v[66:67] op_sel_hi:[1,0]
	v_pk_mul_f32 v[20:21], v[20:21], v[66:67] op_sel_hi:[1,0]
	v_pk_mul_f32 v[22:23], v[22:23], v[66:67] op_sel_hi:[1,0]
	v_pk_mul_f32 v[24:25], v[24:25], v[66:67] op_sel_hi:[1,0]
	v_pk_mul_f32 v[26:27], v[26:27], v[66:67] op_sel_hi:[1,0]
	v_pk_mul_f32 v[28:29], v[28:29], v[66:67] op_sel_hi:[1,0]
	v_pk_mul_f32 v[30:31], v[30:31], v[66:67] op_sel_hi:[1,0]
	v_pk_mul_f32 v[32:33], v[32:33], v[66:67] op_sel_hi:[1,0]
	v_pk_mul_f32 v[6:7], v[6:7], v[66:67] op_sel_hi:[1,0]
	v_pk_mul_f32 v[8:9], v[8:9], v[66:67] op_sel_hi:[1,0]
	v_pk_mul_f32 v[10:11], v[10:11], v[66:67] op_sel_hi:[1,0]
	v_pk_mul_f32 v[12:13], v[12:13], v[66:67] op_sel_hi:[1,0]
	v_pk_mul_f32 v[14:15], v[14:15], v[66:67] op_sel_hi:[1,0]
	v_pk_mul_f32 v[16:17], v[16:17], v[66:67] op_sel_hi:[1,0]
	v_lshl_add_u64 v[66:67], v[68:69], 0, v[0:1]
	v_cvt_pk_bf16_f32 v2, v2, v3
	v_cvt_pk_bf16_f32 v3, v4, v5
	v_cvt_pk_bf16_f32 v4, v18, v19
	v_cvt_pk_bf16_f32 v5, v20, v21
	global_store_dwordx2 v[66:67], v[2:3], off offset:1536
	global_store_dwordx2 v[66:67], v[4:5], off offset:1600
	v_cvt_pk_bf16_f32 v2, v6, v7
	v_cvt_pk_bf16_f32 v3, v8, v9
	v_cvt_pk_bf16_f32 v4, v22, v23
	v_cvt_pk_bf16_f32 v5, v24, v25
	global_store_dwordx2 v[66:67], v[2:3], off offset:1552
	global_store_dwordx2 v[66:67], v[4:5], off offset:1616
	v_cvt_pk_bf16_f32 v2, v10, v11
	v_cvt_pk_bf16_f32 v3, v12, v13
	v_pk_mul_f32 v[34:35], v[34:35], v[70:71] op_sel_hi:[1,0]
	v_pk_mul_f32 v[36:37], v[36:37], v[70:71] op_sel_hi:[1,0]
	v_cvt_pk_bf16_f32 v4, v26, v27
	v_cvt_pk_bf16_f32 v5, v28, v29
	global_store_dwordx2 v[66:67], v[2:3], off offset:1568
	global_store_dwordx2 v[66:67], v[4:5], off offset:1632
	v_cvt_pk_bf16_f32 v2, v14, v15
	v_cvt_pk_bf16_f32 v3, v16, v17
	v_pk_mul_f32 v[50:51], v[50:51], v[70:71] op_sel_hi:[1,0]
	v_pk_mul_f32 v[52:53], v[52:53], v[70:71] op_sel_hi:[1,0]
	v_pk_mul_f32 v[38:39], v[38:39], v[70:71] op_sel_hi:[1,0]
	v_pk_mul_f32 v[40:41], v[40:41], v[70:71] op_sel_hi:[1,0]
	v_cvt_pk_bf16_f32 v4, v30, v31
	v_cvt_pk_bf16_f32 v5, v32, v33
	global_store_dwordx2 v[66:67], v[2:3], off offset:1584
	global_store_dwordx2 v[66:67], v[4:5], off offset:1648
	v_cvt_pk_bf16_f32 v2, v34, v35
	v_cvt_pk_bf16_f32 v3, v36, v37
	v_pk_mul_f32 v[54:55], v[54:55], v[70:71] op_sel_hi:[1,0]
	v_pk_mul_f32 v[56:57], v[56:57], v[70:71] op_sel_hi:[1,0]
	v_pk_mul_f32 v[42:43], v[42:43], v[70:71] op_sel_hi:[1,0]
	v_pk_mul_f32 v[44:45], v[44:45], v[70:71] op_sel_hi:[1,0]
	v_cvt_pk_bf16_f32 v4, v50, v51
	v_cvt_pk_bf16_f32 v5, v52, v53
	global_store_dwordx2 v[66:67], v[2:3], off offset:1664
	global_store_dwordx2 v[66:67], v[4:5], off offset:1728
	v_cvt_pk_bf16_f32 v2, v38, v39
	v_cvt_pk_bf16_f32 v3, v40, v41
	v_pk_mul_f32 v[58:59], v[58:59], v[70:71] op_sel_hi:[1,0]
	v_pk_mul_f32 v[60:61], v[60:61], v[70:71] op_sel_hi:[1,0]
	v_pk_mul_f32 v[46:47], v[46:47], v[70:71] op_sel_hi:[1,0]
	v_pk_mul_f32 v[48:49], v[48:49], v[70:71] op_sel_hi:[1,0]
	v_cvt_pk_bf16_f32 v4, v54, v55
	v_cvt_pk_bf16_f32 v5, v56, v57
	global_store_dwordx2 v[66:67], v[2:3], off offset:1680
	global_store_dwordx2 v[66:67], v[4:5], off offset:1744
	v_cvt_pk_bf16_f32 v2, v42, v43
	v_cvt_pk_bf16_f32 v3, v44, v45
	v_pk_mul_f32 v[62:63], v[62:63], v[70:71] op_sel_hi:[1,0]
	v_pk_mul_f32 v[64:65], v[64:65], v[70:71] op_sel_hi:[1,0]
	v_cvt_pk_bf16_f32 v4, v58, v59
	v_cvt_pk_bf16_f32 v5, v60, v61
	global_store_dwordx2 v[66:67], v[2:3], off offset:1696
	global_store_dwordx2 v[66:67], v[4:5], off offset:1760
	v_cvt_pk_bf16_f32 v2, v46, v47
	v_cvt_pk_bf16_f32 v3, v48, v49
	v_cvt_pk_bf16_f32 v4, v62, v63
	v_cvt_pk_bf16_f32 v5, v64, v65
	global_store_dwordx2 v[66:67], v[2:3], off offset:1712
	global_store_dwordx2 v[66:67], v[4:5], off offset:1776
	s_branch .LBB0_965
